# MLP1 preamble: the 3 per-unit parameter fetch rounds issue all loads first, wait once
# speedup vs baseline: 1.0105x; 1.0006x over previous
.LBB5_5:
	s_abs_i32 s30, s51
	v_cvt_f32_u32_e32 v1, s30
	s_sub_i32 s28, 0, s30
	s_ashr_i32 s23, s6, 3
	s_add_i32 s22, s22, s23
	v_rcp_iflag_f32_e32 v1, v1
	s_abs_i32 s25, s22
	s_ashr_i32 s23, s22, 31
	s_ashr_i32 s34, s51, 31
	v_mul_f32_e32 v1, 0x4f7ffffe, v1
	v_cvt_u32_f32_e32 v1, v1
	s_add_i32 s24, 0, 0x24000
	s_xor_b32 s23, s23, s34
	s_movk_i32 s4, 0xff
	v_readfirstlane_b32 s36, v1
	s_mul_i32 s28, s28, s36
	s_mul_hi_u32 s28, s36, s28
	s_add_i32 s36, s36, s28
	s_mul_hi_u32 s28, s25, s36
	s_mul_i32 s29, s28, s30
	s_sub_i32 s25, s25, s29
	s_add_i32 s29, s28, 1
	s_sub_i32 s38, s25, s30
	s_cmp_ge_u32 s25, s30
	s_cselect_b32 s28, s29, s28
	s_cselect_b32 s25, s38, s25
	s_add_i32 s29, s28, 1
	s_cmp_ge_u32 s25, s30
	s_cselect_b32 s25, s29, s28
	s_xor_b32 s25, s25, s23
	s_sub_i32 s23, s25, s23
	s_lshl_b32 s29, s23, 3
	s_sub_i32 s25, s33, s29
	s_min_i32 s38, s25, 8
	s_abs_i32 s25, s38
	v_cvt_f32_u32_e32 v3, s25
	v_mov_b32_e32 v1, 0xfffffe00
	v_lshl_add_u32 v2, v0, 1, v1
	v_lshl_add_u32 v1, v0, 3, s24
	v_rcp_iflag_f32_e32 v3, v3
	s_sub_i32 s24, 0, s25
	s_mul_i32 s23, s23, s51
	s_sub_i32 s40, s22, s23
	v_mul_f32_e32 v3, 0x4f7ffffe, v3
	v_cvt_u32_f32_e32 v3, v3
	s_abs_i32 s23, s40
	s_xor_b32 s22, s40, s38
	s_ashr_i32 s22, s22, 31
	v_readfirstlane_b32 s28, v3
	s_mul_i32 s24, s24, s28
	s_mul_hi_u32 s24, s28, s24
	s_add_i32 s28, s28, s24
	s_mul_hi_u32 s24, s23, s28
	s_mul_i32 s28, s24, s25
	s_sub_i32 s23, s23, s28
	s_add_i32 s28, s24, 1
	s_sub_i32 s41, s23, s25
	s_cmp_ge_u32 s23, s25
	s_cselect_b32 s24, s28, s24
	s_cselect_b32 s23, s41, s23
	s_add_i32 s28, s24, 1
	s_cmp_ge_u32 s23, s25
	s_cselect_b32 s23, s28, s24
	v_cmp_lt_u32_e64 s[6:7], s4, v0
	s_movk_i32 s4, 0x180
	s_xor_b32 s23, s23, s22
	v_cmp_gt_u32_e64 s[4:5], s4, v0
	s_sub_i32 s28, s23, s22
	s_mul_i32 s44, s28, s38
	s_sub_i32 s44, s40, s44
	s_add_i32 s44, s44, s29
	s_mov_b32 s45, s28
	s_add_u32 s22, s3, s2
	s_addc_u32 s23, s31, s35
	s_ashr_i32 s24, s22, 31
	s_lshr_b32 s24, s24, 29
	s_add_i32 s29, s22, s24
	s_and_b32 s24, s29, -8
	s_sub_i32 s28, s22, s24
	s_cmp_lt_i32 s28, s39
	s_cbranch_scc1 .LBB5_14
	s_sub_i32 s24, s28, s39
	s_mul_i32 s24, s24, s37
	s_add_i32 s38, s24, s52
	s_ashr_i32 s24, s29, 3
	s_cbranch_execz .LBB5_15
	s_branch .LBB5_16

.LBB5_16:
	s_add_i32 s24, s38, s24
	s_abs_i32 s28, s24
	s_mul_hi_u32 s29, s28, s36
	s_mul_i32 s38, s29, s30
	s_ashr_i32 s25, s24, 31
	s_sub_i32 s28, s28, s38
	s_xor_b32 s25, s25, s34
	s_add_i32 s38, s29, 1
	s_sub_i32 s40, s28, s30
	s_cmp_ge_u32 s28, s30
	s_cselect_b32 s29, s38, s29
	s_cselect_b32 s28, s40, s28
	s_add_i32 s38, s29, 1
	s_cmp_ge_u32 s28, s30
	s_cselect_b32 s28, s38, s29
	s_xor_b32 s28, s28, s25
	s_sub_i32 s25, s28, s25
	s_lshl_b32 s40, s25, 3
	s_sub_i32 s28, s33, s40
	s_min_i32 s41, s28, 8
	s_abs_i32 s28, s41
	v_cvt_f32_u32_e32 v3, s28
	s_sub_i32 s29, 0, s28
	s_mul_i32 s25, s25, s51
	s_sub_i32 s42, s24, s25
	v_rcp_iflag_f32_e32 v3, v3
	s_abs_i32 s25, s42
	s_xor_b32 s24, s42, s41
	s_ashr_i32 s24, s24, 31
	v_mul_f32_e32 v3, 0x4f7ffffe, v3
	v_cvt_u32_f32_e32 v3, v3
	s_nop 0
	v_readfirstlane_b32 s38, v3
	s_mul_i32 s29, s29, s38
	s_mul_hi_u32 s29, s38, s29
	s_add_i32 s38, s38, s29
	s_mul_hi_u32 s29, s25, s38
	s_mul_i32 s38, s29, s28
	s_sub_i32 s25, s25, s38
	s_add_i32 s38, s29, 1
	s_sub_i32 s43, s25, s28
	s_cmp_ge_u32 s25, s28
	s_cselect_b32 s29, s38, s29
	s_cselect_b32 s25, s43, s25
	s_add_i32 s38, s29, 1
	s_cmp_ge_u32 s25, s28
	s_cselect_b32 s25, s38, s29
	s_xor_b32 s25, s25, s24
	s_sub_i32 s38, s25, s24
	s_mul_i32 s46, s38, s41
	s_sub_i32 s46, s42, s46
	s_add_i32 s46, s46, s40
	s_mov_b32 s47, s38
	s_add_u32 s22, s22, s3
	s_addc_u32 s23, s23, s31
	s_ashr_i32 s23, s22, 31
	s_lshr_b32 s23, s23, 29
	s_add_i32 s25, s22, s23
	s_and_b32 s23, s25, -8
	s_sub_i32 s24, s22, s23
	s_cmp_lt_i32 s24, s39
	s_cbranch_scc1 .LBB5_25
	s_sub_i32 s22, s24, s39
	s_mul_i32 s22, s22, s37
	s_add_i32 s28, s22, s52
	s_ashr_i32 s22, s25, 3
	s_cbranch_execz .LBB5_26
	s_branch .LBB5_27

.LBB5_27:
	s_add_i32 s22, s28, s22
	s_abs_i32 s24, s22
	s_mul_hi_u32 s25, s24, s36
	s_mul_i32 s28, s25, s30
	s_ashr_i32 s23, s22, 31
	s_sub_i32 s24, s24, s28
	s_xor_b32 s23, s23, s34
	s_add_i32 s28, s25, 1
	s_sub_i32 s29, s24, s30
	s_cmp_ge_u32 s24, s30
	s_cselect_b32 s25, s28, s25
	s_cselect_b32 s24, s29, s24
	s_add_i32 s28, s25, 1
	s_cmp_ge_u32 s24, s30
	s_cselect_b32 s24, s28, s25
	s_xor_b32 s24, s24, s23
	s_sub_i32 s23, s24, s23
	s_lshl_b32 s25, s23, 3
	s_sub_i32 s24, s33, s25
	s_min_i32 s28, s24, 8
	s_abs_i32 s24, s28
	v_cvt_f32_u32_e32 v3, s24
	s_sub_i32 s30, 0, s24
	s_mul_i32 s23, s23, s51
	s_sub_i32 s29, s22, s23
	v_rcp_iflag_f32_e32 v3, v3
	s_abs_i32 s23, s29
	s_xor_b32 s22, s29, s28
	s_ashr_i32 s22, s22, 31
	v_mul_f32_e32 v3, 0x4f7ffffe, v3
	v_cvt_u32_f32_e32 v3, v3
	s_nop 0
	v_readfirstlane_b32 s34, v3
	s_mul_i32 s30, s30, s34
	s_mul_hi_u32 s30, s34, s30
	s_add_i32 s34, s34, s30
	s_mul_hi_u32 s30, s23, s34
	s_mul_i32 s34, s30, s24
	s_sub_i32 s23, s23, s34
	s_add_i32 s34, s30, 1
	s_sub_i32 s36, s23, s24
	s_cmp_ge_u32 s23, s24
	s_cselect_b32 s30, s34, s30
	s_cselect_b32 s23, s36, s23
	s_add_i32 s34, s30, 1
	s_cmp_ge_u32 s23, s24
	s_cselect_b32 s23, s34, s30
	s_xor_b32 s23, s23, s22
	s_sub_i32 s24, s23, s22
	s_mul_i32 s48, s24, s28
	s_sub_i32 s48, s29, s48
	s_add_i32 s48, s48, s25
	s_mov_b32 s49, s24
	s_mov_b32 s40, 0x3aaaaaab
	s_mov_b32 s41, 0x800000
	s_and_saveexec_b64 s[22:23], s[6:7]
	s_xor_b64 s[22:23], exec, s[22:23]
	s_cbranch_execz .Lp1_a
	s_and_saveexec_b64 s[24:25], s[4:5]
	s_cbranch_execz .Lp1_b
	v_lshl_add_u32 v4, s44, 8, v2
	v_ashrrev_i32_e32 v5, 31, v4
	v_lshl_add_u64 v[4:5], v[4:5], 2, s[20:21]
	global_load_dwordx2 v[8:9], v[4:5], off
	v_lshl_add_u32 v4, s46, 8, v2
	v_ashrrev_i32_e32 v5, 31, v4
	v_lshl_add_u64 v[4:5], v[4:5], 2, s[20:21]
	global_load_dwordx2 v[10:11], v[4:5], off
	v_lshl_add_u32 v4, s48, 8, v2
	v_ashrrev_i32_e32 v5, 31, v4
	v_lshl_add_u64 v[4:5], v[4:5], 2, s[20:21]
	global_load_dwordx2 v[12:13], v[4:5], off
	s_waitcnt vmcnt(2)
	v_pk_mul_f32 v[8:9], v[8:9], s[40:41] op_sel_hi:[1,0]
	s_nop 0
	v_fma_f32 v3, -v8, v8, v9
	v_add_f32_e32 v3, 0x3727c5ac, v3
	v_mul_f32_e32 v5, 0x4b800000, v3
	v_cmp_gt_f32_e32 vcc, s41, v3
	s_nop 1
	v_cndmask_b32_e32 v3, v3, v5, vcc
	v_rsq_f32_e32 v3, v3
	s_nop 0
	v_mul_f32_e32 v5, 0x45800000, v3
	v_cndmask_b32_e32 v9, v3, v5, vcc
	ds_write_b64 v1, v[8:9]
	s_waitcnt vmcnt(1)
	v_pk_mul_f32 v[10:11], v[10:11], s[40:41] op_sel_hi:[1,0]
	s_nop 0
	v_fma_f32 v3, -v10, v10, v11
	v_add_f32_e32 v3, 0x3727c5ac, v3
	v_mul_f32_e32 v5, 0x4b800000, v3
	v_cmp_gt_f32_e32 vcc, s41, v3
	s_nop 1
	v_cndmask_b32_e32 v3, v3, v5, vcc
	v_rsq_f32_e32 v3, v3
	s_nop 0
	v_mul_f32_e32 v5, 0x45800000, v3
	v_cndmask_b32_e32 v11, v3, v5, vcc
	ds_write_b64 v1, v[10:11] offset:3072
	s_waitcnt vmcnt(0)
	v_pk_mul_f32 v[12:13], v[12:13], s[40:41] op_sel_hi:[1,0]
	s_nop 0
	v_fma_f32 v3, -v12, v12, v13
	v_add_f32_e32 v3, 0x3727c5ac, v3
	v_mul_f32_e32 v5, 0x4b800000, v3
	v_cmp_gt_f32_e32 vcc, s41, v3
	s_nop 1
	v_cndmask_b32_e32 v3, v3, v5, vcc
	v_rsq_f32_e32 v3, v3
	s_nop 0
	v_mul_f32_e32 v5, 0x45800000, v3
	v_cndmask_b32_e32 v13, v3, v5, vcc
	ds_write_b64 v1, v[12:13] offset:6144

.Lp1_a:
	s_andn2_saveexec_b64 s[22:23], s[22:23]
	s_cbranch_execz .Lp1_c
	v_lshl_or_b32 v4, s45, 8, v0
	v_ashrrev_i32_e32 v5, 31, v4
	v_lshlrev_b64 v[4:5], 2, v[4:5]
	v_lshl_add_u64 v[6:7], s[10:11], 0, v[4:5]
	global_load_dword v8, v[6:7], off
	v_lshl_add_u64 v[6:7], s[12:13], 0, v[4:5]
	global_load_dword v9, v[6:7], off
	v_lshl_add_u64 v[6:7], s[14:15], 0, v[4:5]
	global_load_dword v10, v[6:7], off
	v_lshl_or_b32 v4, s47, 8, v0
	v_ashrrev_i32_e32 v5, 31, v4
	v_lshlrev_b64 v[4:5], 2, v[4:5]
	v_lshl_add_u64 v[6:7], s[10:11], 0, v[4:5]
	global_load_dword v11, v[6:7], off
	v_lshl_add_u64 v[6:7], s[12:13], 0, v[4:5]
	global_load_dword v12, v[6:7], off
	v_lshl_add_u64 v[6:7], s[14:15], 0, v[4:5]
	global_load_dword v13, v[6:7], off
	v_lshl_or_b32 v4, s49, 8, v0
	v_ashrrev_i32_e32 v5, 31, v4
	v_lshlrev_b64 v[4:5], 2, v[4:5]
	v_lshl_add_u64 v[6:7], s[10:11], 0, v[4:5]
	global_load_dword v14, v[6:7], off
	v_lshl_add_u64 v[6:7], s[12:13], 0, v[4:5]
	global_load_dword v15, v[6:7], off
	v_lshl_add_u64 v[6:7], s[14:15], 0, v[4:5]
	global_load_dword v16, v[6:7], off
	v_lshl_add_u32 v5, v0, 2, 0
	s_waitcnt vmcnt(6)
	v_add_u32_e32 v7, 0x24000, v5
	ds_write_b32 v7, v8
	v_add_f32_e32 v3, v9, v10
	v_add_u32_e32 v4, 0x24400, v5
	ds_write_b32 v4, v3
	s_waitcnt vmcnt(3)
	v_add_u32_e32 v7, 0x24c00, v5
	ds_write_b32 v7, v11
	v_add_f32_e32 v3, v12, v13
	v_add_u32_e32 v4, 0x25000, v5
	ds_write_b32 v4, v3
	s_waitcnt vmcnt(0)
	v_add_u32_e32 v7, 0x25800, v5
	ds_write_b32 v7, v14
	v_add_f32_e32 v3, v15, v16
	v_add_u32_e32 v4, 0x25c00, v5
	ds_write_b32 v4, v3
.Lp1_c:
	s_or_b64 exec, exec, s[22:23]
.LBB5_34:
	s_andn2_b64 vcc, exec, s[16:17]
	v_readfirstlane_b32 s29, v0
	s_waitcnt lgkmcnt(0)
	s_barrier
	s_cbranch_vccnz .LBB5_59
	s_ashr_i32 s5, s2, 31
	s_load_dword s4, s[0:1], 0x20
	s_lshr_b32 s5, s5, 29
	s_add_i32 s10, s2, s5
	s_and_b32 s5, s10, -8
	s_sub_i32 s5, s2, s5
	s_cmp_ge_i32 s5, s39
	s_cbranch_scc0 .LBB5_37
	s_sub_i32 s6, s5, s39
	s_mul_i32 s6, s6, s37
	s_add_i32 s22, s6, s52
	s_load_dwordx4 s[12:15], s[0:1], 0x0
	s_ashr_i32 s23, s10, 3
	s_cbranch_execz .LBB5_38
	s_branch .LBB5_39
